# conversion split boundary 0x7e00: 12288 more expert-weight items per layer converted in the idle second round of the router GEMM phase (second timing)
# speedup vs baseline: 1.0116x; 1.0019x over previous
; #define LAS __attribute__((address_space(3)))
; #define REP(k) for (int _rep = 0; _rep < (((PROBE_MASK >> (k)) & 1) ? 2 : 1); ++_rep)
; __device__ __forceinline__ void p_expert_weights(Frame& F, int l, int it0, int it1, int nw, int w) {
;     LAS float* scr = (LAS float*)(F.lds + F.wave * 16384);
;     constexpr int I1 = 16 * 8, I2 = 4 * 32, PER_E = 2 * I1 + I2;
;     for (int it = it0 + w; it < it1; it += nw) {
; __global__ void __launch_bounds__(NTHR, 2) mk_fwd(Args args) {
;     ...
;             REP(0) { p_expert_weights(F, l, (last || F.G != 256) ? 0 : XW_TAIL_G, XW_ITEMS, F.G * NWAVES, F.wg * NWAVES + F.wave); __syncthreads(); }
.Lpa_body:
	v_readlane_b32 s36, v252, 8
	v_readlane_b32 s37, v252, 9
	s_mov_b32 s20, s97
	v_readlane_b32 s38, v252, 10
	v_readlane_b32 s39, v252, 11
	s_mov_b64 s[2:3], s[36:37]
	s_waitcnt vmcnt(0)
	v_mbcnt_lo_u32_b32 v6, -1, 0
	v_mbcnt_hi_u32_b32 v6, -1, v6
	s_nop 0
	v_readlane_b32 s2, v255, 30
	v_readlane_b32 s3, v255, 31
	s_or_b64 s[2:3], s[12:13], s[2:3]
	s_and_b64 s[2:3], s[2:3], exec
	s_cselect_b32 s0, 0, 0x7e00
	v_readlane_b32 s2, v254, 28
	s_add_i32 s0, s0, s2
	s_add_i32 s21, s0, s20
	s_cmp_eq_u32 s100, 1
	s_cselect_b32 s21, 0x10000, s21
	s_cmp_gt_i32 s21, 0xc17f
	s_cbranch_scc1 .LBB0_279
	s_lshl_b32 s0, s20, 14
	s_mov_b32 s31, s23
	s_add_i32 s0, s0, 0
	s_lshl_b64 s[2:3], s[30:31], 20
	s_lshl_b64 s[40:41], s[30:31], 27
	s_add_u32 s50, s38, 0x5900000
	s_addc_u32 s51, s39, 0
	s_add_u32 s52, s38, 0xda00000
	v_readlane_b32 s56, v252, 16
	s_addc_u32 s53, s39, 0
	v_readlane_b32 s57, v252, 17
	v_readlane_b32 s58, v252, 18
	v_readlane_b32 s59, v252, 19
	v_readlane_b32 s60, v252, 20
	v_readlane_b32 s61, v252, 21
	v_readlane_b32 s62, v252, 22
	v_readlane_b32 s63, v252, 23
	v_readlane_b32 s68, v252, 28
	v_lshlrev_b32_e32 v3, 5, v6
	v_readlane_b32 s69, v252, 29
	s_add_u32 s54, s68, s40
	v_readlane_b32 s56, v252, 0
	v_ashrrev_i32_e32 v7, 5, v6
	v_and_b32_e32 v0, 31, v6
	s_movk_i32 s4, 0x84
	v_ashrrev_i32_e32 v8, 1, v6
	v_and_b32_e32 v4, 32, v3
	s_addc_u32 s55, s69, s41
	v_readlane_b32 s58, v252, 2
	v_lshl_add_u32 v1, v0, 2, s0
	v_mul_lo_u32 v2, v7, s4
	v_mul_u32_u24_e32 v3, 0x84, v4
	v_lshlrev_b32_e32 v5, 2, v8
	v_readlane_b32 s57, v252, 1
	v_readlane_b32 s59, v252, 3
	v_readlane_b32 s60, v252, 4
	v_readlane_b32 s61, v252, 5
	s_add_u32 s56, s58, s2
	s_waitcnt lgkmcnt(0)
	v_add3_u32 v9, s0, v3, v5
	v_readlane_b32 s4, v255, 14
	v_add_u32_e32 v10, v1, v2
	s_addc_u32 s57, s59, s3
	v_mov_b32_e32 v5, v193
	s_lshl_b32 s58, s21, 5
	s_lshl_b32 s59, s4, 5
	s_lshl_b32 s60, s21, 1
	s_lshl_b32 s61, s4, 1
	v_lshlrev_b32_e32 v192, 2, v0
	v_add_u32_e32 v11, 0x400, v10
	v_add_u32_e32 v12, 0x800, v10
	v_add_u32_e32 v13, 0xc00, v10
	v_add_u32_e32 v14, 0x1000, v10
	v_add_u32_e32 v15, 0x1400, v10
	v_add_u32_e32 v16, 0x1800, v10
	v_add_u32_e32 v17, 0x1c00, v10
	v_add_u32_e32 v18, 0x400, v9
	v_add_u32_e32 v19, 0x800, v9
	v_add_u32_e32 v20, 0xc00, v9
	v_readlane_b32 s64, v252, 24
	v_readlane_b32 s65, v252, 25
	v_readlane_b32 s66, v252, 26
	v_readlane_b32 s67, v252, 27
	v_readlane_b32 s70, v252, 30
	v_readlane_b32 s71, v252, 31
	v_readlane_b32 s62, v252, 6
	v_readlane_b32 s63, v252, 7
	v_readlane_b32 s5, v255, 15
	s_branch .LBB0_272

; #define LAS __attribute__((address_space(3)))
; __device__ __forceinline__ void p_expert_weights(Frame& F, int l, int it0, int it1, int nw, int w) {
;     LAS float* scr = (LAS float*)(F.lds + F.wave * 16384);
;     constexpr int I1 = 16 * 8, I2 = 4 * 32, PER_E = 2 * I1 + I2;
;     for (int it = it0 + w; it < it1; it += nw) {
; __global__ void __launch_bounds__(NTHR, 2) mk_fwd(Args args) {
;     ...
;             if (!last && F.G == 256 && F.wg >= 16) { __syncthreads(); FRESH(); p_expert_weights(F, l, XW_TAIL_E, XW_TAIL_G, 240 * NWAVES, (F.wg - 16) * NWAVES + F.wave); }
.LBB0_853:
	v_readlane_b32 s2, v255, 30
	v_readlane_b32 s3, v255, 31
	v_readlane_b32 s4, v254, 21
	s_xor_b64 s[2:3], s[2:3], -1
	v_readlane_b32 s5, v254, 22
	s_and_b64 s[2:3], s[2:3], s[4:5]
	v_readlane_b32 s4, v254, 26
	v_readlane_b32 s5, v254, 27
	s_and_b64 s[2:3], s[4:5], s[2:3]
	s_andn2_b64 vcc, exec, s[2:3]
	s_cbranch_vccnz .LBB0_861
	v_readlane_b32 s36, v252, 8
	v_readlane_b32 s37, v252, 9
	v_readlane_b32 s38, v252, 10
	v_readlane_b32 s39, v252, 11
	s_mov_b32 s0, s97
	s_mov_b64 s[2:3], s[38:39]
	s_mov_b64 s[4:5], s[36:37]
	s_waitcnt vmcnt(0) lgkmcnt(0)
	s_barrier
	v_mbcnt_lo_u32_b32 v0, -1, 0
	v_mbcnt_hi_u32_b32 v0, -1, v0
	s_nop 0
	v_readlane_b32 s4, v254, 29
	s_add_i32 s4, s4, s0
	s_cmpk_gt_i32 s4, 0x4dff
	s_cbranch_scc1 .LBB0_861
	s_lshl_b32 s0, s0, 14
	s_add_i32 s0, s0, 0
	s_add_i32 s38, s4, 0x3000
	s_lshl_b32 s18, s30, 27
	s_add_u32 s19, s2, 0xda00000
	v_readlane_b32 s40, v252, 16
	s_addc_u32 s39, s3, 0
	v_readlane_b32 s52, v252, 28
	v_readlane_b32 s41, v252, 17
	v_readlane_b32 s53, v252, 29
	s_add_u32 s40, s52, s18
	v_ashrrev_i32_e32 v5, 5, v0
	v_and_b32_e32 v4, 31, v0
	v_ashrrev_i32_e32 v8, 1, v0
	v_lshlrev_b32_e32 v0, 5, v0
	v_readlane_b32 s42, v252, 18
	s_addc_u32 s41, s53, 0
	s_movk_i32 s4, 0x84
	v_and_b32_e32 v6, 32, v0
	v_readlane_b32 s43, v252, 19
	v_readlane_b32 s44, v252, 20
	v_readlane_b32 s45, v252, 21
	v_lshl_add_u32 v1, v4, 2, s0
	v_mul_lo_u32 v2, v5, s4
	v_mul_u32_u24_e32 v0, 0x84, v6
	v_lshlrev_b32_e32 v3, 2, v8
	s_add_u32 s42, s2, 0x5900000
	v_add3_u32 v9, s0, v0, v3
	v_mov_b32_e32 v7, v193
	s_addc_u32 s43, s3, 0
	s_lshl_b32 s44, s38, 5
	s_lshl_b32 s45, s38, 1
	v_add_u32_e32 v10, v1, v2
	v_readlane_b32 s46, v252, 22
	v_readlane_b32 s47, v252, 23
	v_readlane_b32 s48, v252, 24
	v_readlane_b32 s49, v252, 25
	v_readlane_b32 s50, v252, 26
	v_readlane_b32 s51, v252, 27
	v_readlane_b32 s54, v252, 30
	v_readlane_b32 s55, v252, 31
	s_branch .LBB0_857
.LBB0_856:
	s_add_i32 s0, s38, 0x780
	s_add_i32 s44, s44, 0xf000
	s_addk_i32 s45, 0xf00
	s_cmpk_lt_i32 s38, 0x7680
	s_mov_b32 s38, s0
	s_cbranch_scc0 .LBB0_861
